# LDS bank conflicts: LSTM h row stride 144 -> 160 bytes so the per-step ds_write_b16 of h hits 16 distinct banks per wave
# speedup vs baseline: 1.0012x; 1.0001x over previous
_Z12lstm2_kernelPKDF16_PKDv8_DF16_Pf:
	s_load_dwordx4 s[8:11], s[0:1], 0x0
	s_load_dwordx2 s[12:13], s[0:1], 0x10
	s_and_b32 s14, s2, 1
	s_lshr_b32 s15, s2, 1
	v_and_b32_e32 v1, 63, v0
	v_lshrrev_b32_e32 v2, 6, v0
	v_lshrrev_b32_e32 v3, 4, v1
	v_and_b32_e32 v4, 15, v0
	v_lshrrev_b32_e32 v5, 2, v4
	v_and_b32_e32 v6, 3, v0
	v_lshlrev_b32_e32 v7, 4, v1
	v_lshl_add_u32 v8, v2, 13, v7
	v_lshl_add_u32 v9, v2, 14, v7
	s_waitcnt lgkmcnt(0)
	s_lshl_b32 s16, s14, 15
	s_add_u32 s16, s16, 0x64000
	s_add_u32 s16, s10, s16
	s_addc_u32 s17, s11, 0
	s_lshl_b32 s18, s14, 16
	s_add_u32 s18, s18, 0x44000
	s_add_u32 s18, s10, s18
	s_addc_u32 s19, s11, 0
	v_add_u32_e32 v10, 0x1000, v8
	global_load_dwordx4 v[16:19], v8, s[16:17] offset:0
	global_load_dwordx4 v[20:23], v8, s[16:17] offset:1024
	global_load_dwordx4 v[24:27], v8, s[16:17] offset:2048
	global_load_dwordx4 v[28:31], v8, s[16:17] offset:3072
	global_load_dwordx4 v[32:35], v10, s[16:17] offset:0
	global_load_dwordx4 v[36:39], v10, s[16:17] offset:1024
	global_load_dwordx4 v[40:43], v10, s[16:17] offset:2048
	global_load_dwordx4 v[44:47], v10, s[16:17] offset:3072
	v_add_u32_e32 v11, 0x1000, v9
	v_add_u32_e32 v12, 0x2000, v9
	v_add_u32_e32 v13, 0x3000, v9
	global_load_dwordx4 v[48:51], v9, s[18:19] offset:0
	global_load_dwordx4 v[52:55], v9, s[18:19] offset:1024
	global_load_dwordx4 v[56:59], v9, s[18:19] offset:2048
	global_load_dwordx4 v[60:63], v9, s[18:19] offset:3072
	global_load_dwordx4 v[64:67], v11, s[18:19] offset:0
	global_load_dwordx4 v[68:71], v11, s[18:19] offset:1024
	global_load_dwordx4 v[72:75], v11, s[18:19] offset:2048
	global_load_dwordx4 v[76:79], v11, s[18:19] offset:3072
	global_load_dwordx4 v[80:83], v12, s[18:19] offset:0
	global_load_dwordx4 v[84:87], v12, s[18:19] offset:1024
	global_load_dwordx4 v[88:91], v12, s[18:19] offset:2048
	global_load_dwordx4 v[92:95], v12, s[18:19] offset:3072
	global_load_dwordx4 v[96:99], v13, s[18:19] offset:0
	global_load_dwordx4 v[100:103], v13, s[18:19] offset:1024
	global_load_dwordx4 v[104:107], v13, s[18:19] offset:2048
	global_load_dwordx4 v[108:111], v13, s[18:19] offset:3072
	s_lshl_b32 s22, s14, 10
	s_add_u32 s22, s8, s22
	s_addc_u32 s23, s9, 0
	v_lshl_add_u32 v14, v2, 4, v3
	v_lshlrev_b32_e32 v14, 2, v14
	global_load_dword v112, v14, s[22:23] offset:0
	global_load_dword v113, v14, s[22:23] offset:256
	global_load_dword v114, v14, s[22:23] offset:512
	global_load_dword v115, v14, s[22:23] offset:768
	global_load_dword v116, v14, s[22:23] offset:16
	global_load_dword v117, v14, s[22:23] offset:272
	global_load_dword v118, v14, s[22:23] offset:528
	global_load_dword v119, v14, s[22:23] offset:784
	global_load_dword v120, v14, s[22:23] offset:32
	global_load_dword v121, v14, s[22:23] offset:288
	global_load_dword v122, v14, s[22:23] offset:544
	global_load_dword v123, v14, s[22:23] offset:800
	global_load_dword v124, v14, s[22:23] offset:48
	global_load_dword v125, v14, s[22:23] offset:304
	global_load_dword v126, v14, s[22:23] offset:560
	global_load_dword v127, v14, s[22:23] offset:816
	s_add_u32 s24, s8, 0xc808000
	s_addc_u32 s25, s9, 0
	s_lshl_b32 s26, s15, 2
	v_add_u32_e32 v15, s26, v6
	s_cmp_eq_u32 s14, 0
	v_sub_u32_e32 v200, 0x18f, v5
	s_cselect_b64 vcc, -1, 0
	s_nop 1
	v_cndmask_b32_e32 v200, v200, v5, vcc
	v_mov_b32_e32 v201, 0x190
	v_mad_u32_u24 v200, v15, v201, v200
	v_lshlrev_b32_e32 v200, 8, v200
	v_lshl_add_u32 v200, v3, 4, v200
	v_mov_b32_e32 v201, 0
	v_lshl_add_u64 v[228:229], s[24:25], 0, v[200:201]
	s_mov_b32 s28, 0x400
	s_cselect_b32 s20, s28, 0xfffffc00
	s_cselect_b32 s21, 0, -1
	global_load_dwordx4 v[128:131], v[228:229], off offset:0
	global_load_dwordx4 v[132:135], v[228:229], off offset:64
	global_load_dwordx4 v[136:139], v[228:229], off offset:128
	global_load_dwordx4 v[140:143], v[228:229], off offset:192
	v_lshl_add_u64 v[228:229], v[228:229], 0, s[20:21]
	global_load_dwordx4 v[144:147], v[228:229], off offset:0
	global_load_dwordx4 v[148:151], v[228:229], off offset:64
	global_load_dwordx4 v[152:155], v[228:229], off offset:128
	global_load_dwordx4 v[156:159], v[228:229], off offset:192
	v_lshl_add_u64 v[228:229], v[228:229], 0, s[20:21]
	v_mul_u32_u24_e32 v202, 160, v6
	v_lshl_add_u32 v224, v3, 4, v202
	v_lshl_add_u32 v203, v2, 4, v3
	v_lshl_add_u32 v203, v5, 2, v203
	v_lshl_add_u32 v225, v203, 1, v202
	v_mul_u32_u24_e32 v204, 8704, v2
	v_lshlrev_b32_e32 v205, 8, v3
	v_lshl_add_u32 v205, v6, 4, v205
	v_add_u32_e32 v205, 1408, v205
	v_add_u32_e32 v205, v205, v204
	v_lshl_add_u32 v226, v5, 6, v205
	v_mul_u32_u24_e32 v206, 1088, v5
	v_add_u32_e32 v227, v205, v206
	v_lshlrev_b32_e32 v206, 4, v3
	v_cmp_gt_u32_e32 vcc, 2, v5
	s_nop 1
	v_add_u32_e32 v208, 1280, v206
	v_cndmask_b32_e32 v209, v208, v224, vcc
	v_cndmask_b32_e32 v211, v224, v208, vcc
	v_add_u32_e32 v208, 640, v206
	v_cndmask_b32_e32 v210, v208, v224, vcc
	v_cndmask_b32_e32 v212, v224, v208, vcc
	s_lshl_b32 s27, s14, 6
	v_lshl_add_u32 v230, v15, 7, v203
	v_add_u32_e32 v230, s27, v230
	v_lshlrev_b32_e32 v230, 2, v230
	v_mov_b32_e32 v208, 0
	v_lshlrev_b32_e32 v200, 2, v0
	v_lshlrev_b32_e32 v201, 2, v1
	ds_write_b32 v200, v208
	ds_write_b32 v201, v208 offset:1024
	v_and_b32_e32 v202, 31, v1
	v_lshlrev_b32_e32 v202, 2, v202
	ds_write_b32 v202, v208 offset:1280
	v_mov_b32_e32 v220, 0
	v_mov_b32_e32 v221, 0xff61b1e6
	v_mov_b32_e32 v222, 0x4038aa3b
	v_mov_b32_e32 v215, 0xff61b1e6
	s_waitcnt vmcnt(0)
	v_mfma_f32_16x16x32_f16 v[168:171], v[48:51], v[128:131], v[112:115]
	v_mfma_f32_16x16x32_f16 v[168:171], v[52:55], v[132:135], v[168:171]
	v_mfma_f32_16x16x32_f16 v[168:171], v[56:59], v[136:139], v[168:171]
	v_mfma_f32_16x16x32_f16 v[168:171], v[60:63], v[140:143], v[168:171]
	v_mfma_f32_16x16x32_f16 v[172:175], v[64:67], v[128:131], v[116:119]
	v_mfma_f32_16x16x32_f16 v[172:175], v[68:71], v[132:135], v[172:175]
	v_mfma_f32_16x16x32_f16 v[172:175], v[72:75], v[136:139], v[172:175]
	v_mfma_f32_16x16x32_f16 v[172:175], v[76:79], v[140:143], v[172:175]
	v_mfma_f32_16x16x32_f16 v[176:179], v[80:83], v[128:131], v[120:123]
	v_mfma_f32_16x16x32_f16 v[176:179], v[84:87], v[132:135], v[176:179]
	v_mfma_f32_16x16x32_f16 v[176:179], v[88:91], v[136:139], v[176:179]
	v_mfma_f32_16x16x32_f16 v[176:179], v[92:95], v[140:143], v[176:179]
	v_mfma_f32_16x16x32_f16 v[180:183], v[96:99], v[128:131], v[124:127]
	v_mfma_f32_16x16x32_f16 v[180:183], v[100:103], v[132:135], v[180:183]
	v_mfma_f32_16x16x32_f16 v[180:183], v[104:107], v[136:139], v[180:183]
	v_mfma_f32_16x16x32_f16 v[180:183], v[108:111], v[140:143], v[180:183]
	v_mfma_f32_16x16x32_f16 v[160:163], v[48:51], v[144:147], v[112:115]
	v_mfma_f32_16x16x32_f16 v[164:167], v[64:67], v[144:147], v[116:119]
	v_mfma_f32_16x16x32_f16 v[160:163], v[52:55], v[148:151], v[160:163]
	v_mfma_f32_16x16x32_f16 v[160:163], v[56:59], v[152:155], v[160:163]
	s_nop 7
	ds_write_b128 v227, v[168:171] offset:0
	ds_write_b128 v227, v[172:175] offset:64
	ds_write_b128 v227, v[176:179] offset:128
	ds_write_b128 v227, v[180:183] offset:192
	global_load_dwordx4 v[128:131], v[228:229], off offset:0
	global_load_dwordx4 v[132:135], v[228:229], off offset:64
	global_load_dwordx4 v[136:139], v[228:229], off offset:128
	global_load_dwordx4 v[140:143], v[228:229], off offset:192
	v_lshl_add_u64 v[228:229], v[228:229], 0, s[20:21]
	s_movk_i32 s4, 50
	s_waitcnt lgkmcnt(0)
	s_barrier
	ds_read_b128 v[192:195], v226 offset:0
.Llstm3_loop:
	ds_read_b128 v[184:187], v209 offset:0
	ds_read_b128 v[188:191], v209 offset:64
	ds_read_b128 v[176:179], v211 offset:0
	ds_read_b128 v[180:183], v211 offset:64
	v_mfma_f32_16x16x32_f16 v[164:167], v[68:71], v[148:151], v[164:167]
	s_waitcnt vmcnt(4)
	v_mfma_f32_16x16x32_f16 v[160:163], v[60:63], v[156:159], v[160:163]
	s_waitcnt lgkmcnt(3)
	v_mfma_f32_16x16x32_f16 v[168:171], v[16:19], v[184:187], v[192:195]
	v_mfma_f32_16x16x32_f16 v[172:175], v[24:27], v[184:187], v[192:195]
	s_waitcnt lgkmcnt(2)
	v_mfma_f32_16x16x32_f16 v[168:171], v[20:23], v[188:191], v[168:171]
	v_mfma_f32_16x16x32_f16 v[172:175], v[28:31], v[188:191], v[172:175]
	s_waitcnt lgkmcnt(1)
	v_mfma_f32_16x16x32_f16 v[168:171], v[32:35], v[176:179], v[168:171]
	v_mfma_f32_16x16x32_f16 v[172:175], v[40:43], v[176:179], v[172:175]
	s_waitcnt lgkmcnt(0)
	v_mfma_f32_16x16x32_f16 v[168:171], v[36:39], v[180:183], v[168:171]
	v_mfma_f32_16x16x32_f16 v[172:175], v[44:47], v[180:183], v[172:175]
	s_nop 7
	v_mov_b32_dpp v168, v172 quad_perm:[0,1,2,3] row_mask:0xf bank_mask:0xa
	v_mov_b32_dpp v169, v173 quad_perm:[0,1,2,3] row_mask:0xf bank_mask:0xa
	v_mov_b32_dpp v170, v174 quad_perm:[0,1,2,3] row_mask:0xf bank_mask:0xa
	v_exp_f32_e32 v200, v168
	v_mov_b32_dpp v171, v175 quad_perm:[0,1,2,3] row_mask:0xf bank_mask:0xa
	v_exp_f32_e32 v201, v169
	v_exp_f32_e32 v202, v170
	v_exp_f32_e32 v203, v171
	v_pk_add_f32 v[200:201], v[200:201], 1.0 op_sel_hi:[1,0]
	v_pk_add_f32 v[202:203], v[202:203], 1.0 op_sel_hi:[1,0]
	v_rcp_f32_e32 v202, v202
	v_rcp_f32_e32 v200, v200
	v_rcp_f32_e32 v201, v201
	v_rcp_f32_e32 v203, v203
	v_fmamk_f32 v204, v202, 0xc0b8aa3b, v222
	v_mul_f32_e32 v205, v200, v204
	v_fma_f32 v220, v201, v220, v205
	v_exp_f32_e32 v206, v220
	v_mul_f32_e32 v207, -2.0, v203
	v_add_f32_e32 v206, 1.0, v206
	v_rcp_f32_e32 v206, v206
	v_max_f32_e32 v221, v221, v215
	v_fma_mixlo_f16 v208, v206, v207, v203
	ds_write_b16 v225, v208 offset:640
	v_fma_f32 v215, v206, v207, v203
	v_mfma_f32_16x16x32_f16 v[232:235], v[80:83], v[144:147], v[120:123]
	v_mfma_f32_16x16x32_f16 v[164:167], v[72:75], v[152:155], v[164:167]
	ds_write_b128 v227, v[160:163] offset:4352
	ds_read_b128 v[196:199], v226 offset:1088
	s_waitcnt lgkmcnt(2)
	s_barrier
	ds_read_b128 v[184:187], v210 offset:640
	ds_read_b128 v[188:191], v210 offset:704
	ds_read_b128 v[176:179], v212 offset:640
	ds_read_b128 v[180:183], v212 offset:704
	v_mfma_f32_16x16x32_f16 v[232:235], v[84:87], v[148:151], v[232:235]
	v_mfma_f32_16x16x32_f16 v[164:167], v[76:79], v[156:159], v[164:167]
	s_waitcnt lgkmcnt(3)
	v_mfma_f32_16x16x32_f16 v[168:171], v[16:19], v[184:187], v[196:199]
	v_mfma_f32_16x16x32_f16 v[172:175], v[24:27], v[184:187], v[196:199]
	s_waitcnt lgkmcnt(2)
	v_mfma_f32_16x16x32_f16 v[168:171], v[20:23], v[188:191], v[168:171]
	v_mfma_f32_16x16x32_f16 v[172:175], v[28:31], v[188:191], v[172:175]
	s_waitcnt lgkmcnt(1)
	v_mfma_f32_16x16x32_f16 v[168:171], v[32:35], v[176:179], v[168:171]
	v_mfma_f32_16x16x32_f16 v[172:175], v[40:43], v[176:179], v[172:175]
	s_waitcnt lgkmcnt(0)
	v_mfma_f32_16x16x32_f16 v[168:171], v[36:39], v[180:183], v[168:171]
	v_mfma_f32_16x16x32_f16 v[172:175], v[44:47], v[180:183], v[172:175]
	s_nop 7
	v_mov_b32_dpp v168, v172 quad_perm:[0,1,2,3] row_mask:0xf bank_mask:0xa
	v_mov_b32_dpp v169, v173 quad_perm:[0,1,2,3] row_mask:0xf bank_mask:0xa
	v_mov_b32_dpp v170, v174 quad_perm:[0,1,2,3] row_mask:0xf bank_mask:0xa
	v_exp_f32_e32 v200, v168
	v_mov_b32_dpp v171, v175 quad_perm:[0,1,2,3] row_mask:0xf bank_mask:0xa
	v_exp_f32_e32 v201, v169
	v_exp_f32_e32 v202, v170
	v_exp_f32_e32 v203, v171
	v_pk_add_f32 v[200:201], v[200:201], 1.0 op_sel_hi:[1,0]
	v_pk_add_f32 v[202:203], v[202:203], 1.0 op_sel_hi:[1,0]
	v_rcp_f32_e32 v202, v202
	v_rcp_f32_e32 v200, v200
	v_rcp_f32_e32 v201, v201
	v_rcp_f32_e32 v203, v203
	v_fmamk_f32 v204, v202, 0xc0b8aa3b, v222
	v_mul_f32_e32 v205, v200, v204
	v_fma_f32 v220, v201, v220, v205
	v_exp_f32_e32 v206, v220
	v_mul_f32_e32 v207, -2.0, v203
	v_add_f32_e32 v206, 1.0, v206
	v_rcp_f32_e32 v206, v206
	v_max_f32_e32 v221, v221, v215
	v_fma_mixlo_f16 v208, v206, v207, v203
	ds_write_b16 v225, v208 offset:0
	v_fma_f32 v215, v206, v207, v203
	v_mfma_f32_16x16x32_f16 v[236:239], v[96:99], v[144:147], v[124:127]
	v_mfma_f32_16x16x32_f16 v[232:235], v[88:91], v[152:155], v[232:235]
	global_load_dwordx4 v[144:147], v[228:229], off offset:0
	ds_write_b128 v227, v[164:167] offset:4416
	ds_read_b128 v[192:195], v226 offset:2176
	s_waitcnt lgkmcnt(2)
	s_barrier
	ds_read_b128 v[184:187], v209 offset:0
	ds_read_b128 v[188:191], v209 offset:64
	ds_read_b128 v[176:179], v211 offset:0
	ds_read_b128 v[180:183], v211 offset:64
	v_mfma_f32_16x16x32_f16 v[236:239], v[100:103], v[148:151], v[236:239]
	v_mfma_f32_16x16x32_f16 v[232:235], v[92:95], v[156:159], v[232:235]
	global_load_dwordx4 v[148:151], v[228:229], off offset:64
	s_waitcnt lgkmcnt(3)
	v_mfma_f32_16x16x32_f16 v[168:171], v[16:19], v[184:187], v[192:195]
	v_mfma_f32_16x16x32_f16 v[172:175], v[24:27], v[184:187], v[192:195]
	s_waitcnt lgkmcnt(2)
	v_mfma_f32_16x16x32_f16 v[168:171], v[20:23], v[188:191], v[168:171]
	v_mfma_f32_16x16x32_f16 v[172:175], v[28:31], v[188:191], v[172:175]
	s_waitcnt lgkmcnt(1)
	v_mfma_f32_16x16x32_f16 v[168:171], v[32:35], v[176:179], v[168:171]
	v_mfma_f32_16x16x32_f16 v[172:175], v[40:43], v[176:179], v[172:175]
	s_waitcnt lgkmcnt(0)
	v_mfma_f32_16x16x32_f16 v[168:171], v[36:39], v[180:183], v[168:171]
	v_mfma_f32_16x16x32_f16 v[172:175], v[44:47], v[180:183], v[172:175]
	s_nop 7
	v_mov_b32_dpp v168, v172 quad_perm:[0,1,2,3] row_mask:0xf bank_mask:0xa
	v_mov_b32_dpp v169, v173 quad_perm:[0,1,2,3] row_mask:0xf bank_mask:0xa
	v_mov_b32_dpp v170, v174 quad_perm:[0,1,2,3] row_mask:0xf bank_mask:0xa
	v_exp_f32_e32 v200, v168
	v_mov_b32_dpp v171, v175 quad_perm:[0,1,2,3] row_mask:0xf bank_mask:0xa
	v_exp_f32_e32 v201, v169
	v_exp_f32_e32 v202, v170
	v_exp_f32_e32 v203, v171
	v_pk_add_f32 v[200:201], v[200:201], 1.0 op_sel_hi:[1,0]
	v_pk_add_f32 v[202:203], v[202:203], 1.0 op_sel_hi:[1,0]
	v_rcp_f32_e32 v202, v202
	v_rcp_f32_e32 v200, v200
	v_rcp_f32_e32 v201, v201
	v_rcp_f32_e32 v203, v203
	v_fmamk_f32 v204, v202, 0xc0b8aa3b, v222
	v_mul_f32_e32 v205, v200, v204
	v_fma_f32 v220, v201, v220, v205
	v_exp_f32_e32 v206, v220
	v_mul_f32_e32 v207, -2.0, v203
	v_add_f32_e32 v206, 1.0, v206
	v_rcp_f32_e32 v206, v206
	v_max_f32_e32 v221, v221, v215
	v_fma_mixlo_f16 v208, v206, v207, v203
	ds_write_b16 v225, v208 offset:640
	v_fma_f32 v215, v206, v207, v203
	s_waitcnt vmcnt(5)
	v_mfma_f32_16x16x32_f16 v[160:163], v[48:51], v[128:131], v[112:115]
	v_mfma_f32_16x16x32_f16 v[236:239], v[104:107], v[152:155], v[236:239]
	global_load_dwordx4 v[152:155], v[228:229], off offset:128
	ds_write_b128 v227, v[232:235] offset:4480
	ds_read_b128 v[196:199], v226 offset:3264
	s_waitcnt lgkmcnt(2)
	s_barrier
	ds_read_b128 v[184:187], v210 offset:640
	ds_read_b128 v[188:191], v210 offset:704
	ds_read_b128 v[176:179], v212 offset:640
	ds_read_b128 v[180:183], v212 offset:704
	s_waitcnt vmcnt(5)
	v_mfma_f32_16x16x32_f16 v[160:163], v[52:55], v[132:135], v[160:163]
	v_mfma_f32_16x16x32_f16 v[236:239], v[108:111], v[156:159], v[236:239]
	global_load_dwordx4 v[156:159], v[228:229], off offset:192
	v_lshl_add_u64 v[228:229], v[228:229], 0, s[20:21]
	s_waitcnt lgkmcnt(3)
	v_mfma_f32_16x16x32_f16 v[168:171], v[16:19], v[184:187], v[196:199]
	v_mfma_f32_16x16x32_f16 v[172:175], v[24:27], v[184:187], v[196:199]
	s_waitcnt lgkmcnt(2)
	v_mfma_f32_16x16x32_f16 v[168:171], v[20:23], v[188:191], v[168:171]
	v_mfma_f32_16x16x32_f16 v[172:175], v[28:31], v[188:191], v[172:175]
	s_waitcnt lgkmcnt(1)
	v_mfma_f32_16x16x32_f16 v[168:171], v[32:35], v[176:179], v[168:171]
	v_mfma_f32_16x16x32_f16 v[172:175], v[40:43], v[176:179], v[172:175]
	s_waitcnt lgkmcnt(0)
	v_mfma_f32_16x16x32_f16 v[168:171], v[36:39], v[180:183], v[168:171]
	v_mfma_f32_16x16x32_f16 v[172:175], v[44:47], v[180:183], v[172:175]
	s_nop 7
	v_mov_b32_dpp v168, v172 quad_perm:[0,1,2,3] row_mask:0xf bank_mask:0xa
	v_mov_b32_dpp v169, v173 quad_perm:[0,1,2,3] row_mask:0xf bank_mask:0xa
	v_mov_b32_dpp v170, v174 quad_perm:[0,1,2,3] row_mask:0xf bank_mask:0xa
	v_exp_f32_e32 v200, v168
	v_mov_b32_dpp v171, v175 quad_perm:[0,1,2,3] row_mask:0xf bank_mask:0xa
	v_exp_f32_e32 v201, v169
	v_exp_f32_e32 v202, v170
	v_exp_f32_e32 v203, v171
	v_pk_add_f32 v[200:201], v[200:201], 1.0 op_sel_hi:[1,0]
	v_pk_add_f32 v[202:203], v[202:203], 1.0 op_sel_hi:[1,0]
	v_rcp_f32_e32 v202, v202
	v_rcp_f32_e32 v200, v200
	v_rcp_f32_e32 v201, v201
	v_rcp_f32_e32 v203, v203
	v_fmamk_f32 v204, v202, 0xc0b8aa3b, v222
	v_mul_f32_e32 v205, v200, v204
	v_fma_f32 v220, v201, v220, v205
	v_exp_f32_e32 v206, v220
	v_mul_f32_e32 v207, -2.0, v203
	v_add_f32_e32 v206, 1.0, v206
	v_rcp_f32_e32 v206, v206
	v_max_f32_e32 v221, v221, v215
	v_fma_mixlo_f16 v208, v206, v207, v203
	ds_write_b16 v225, v208 offset:0
	v_fma_f32 v215, v206, v207, v203
	v_mfma_f32_16x16x32_f16 v[164:167], v[64:67], v[128:131], v[116:119]
	s_waitcnt vmcnt(5)
	v_mfma_f32_16x16x32_f16 v[160:163], v[56:59], v[136:139], v[160:163]
	ds_write_b128 v227, v[236:239] offset:4544
	ds_read_b128 v[192:195], v226 offset:4352
	s_waitcnt lgkmcnt(2)
	s_barrier
	ds_read_b128 v[184:187], v209 offset:0
	ds_read_b128 v[188:191], v209 offset:64
	ds_read_b128 v[176:179], v211 offset:0
	ds_read_b128 v[180:183], v211 offset:64
	v_mfma_f32_16x16x32_f16 v[164:167], v[68:71], v[132:135], v[164:167]
	s_waitcnt vmcnt(4)
	v_mfma_f32_16x16x32_f16 v[160:163], v[60:63], v[140:143], v[160:163]
	s_waitcnt lgkmcnt(3)
	v_mfma_f32_16x16x32_f16 v[168:171], v[16:19], v[184:187], v[192:195]
	v_mfma_f32_16x16x32_f16 v[172:175], v[24:27], v[184:187], v[192:195]
	s_waitcnt lgkmcnt(2)
	v_mfma_f32_16x16x32_f16 v[168:171], v[20:23], v[188:191], v[168:171]
	v_mfma_f32_16x16x32_f16 v[172:175], v[28:31], v[188:191], v[172:175]
	s_waitcnt lgkmcnt(1)
	v_mfma_f32_16x16x32_f16 v[168:171], v[32:35], v[176:179], v[168:171]
	v_mfma_f32_16x16x32_f16 v[172:175], v[40:43], v[176:179], v[172:175]
	s_waitcnt lgkmcnt(0)
	v_mfma_f32_16x16x32_f16 v[168:171], v[36:39], v[180:183], v[168:171]
	v_mfma_f32_16x16x32_f16 v[172:175], v[44:47], v[180:183], v[172:175]
	s_nop 7
	v_mov_b32_dpp v168, v172 quad_perm:[0,1,2,3] row_mask:0xf bank_mask:0xa
	v_mov_b32_dpp v169, v173 quad_perm:[0,1,2,3] row_mask:0xf bank_mask:0xa
	v_mov_b32_dpp v170, v174 quad_perm:[0,1,2,3] row_mask:0xf bank_mask:0xa
	v_exp_f32_e32 v200, v168
	v_mov_b32_dpp v171, v175 quad_perm:[0,1,2,3] row_mask:0xf bank_mask:0xa
	v_exp_f32_e32 v201, v169
	v_exp_f32_e32 v202, v170
	v_exp_f32_e32 v203, v171
	v_pk_add_f32 v[200:201], v[200:201], 1.0 op_sel_hi:[1,0]
	v_pk_add_f32 v[202:203], v[202:203], 1.0 op_sel_hi:[1,0]
	v_rcp_f32_e32 v202, v202
	v_rcp_f32_e32 v200, v200
	v_rcp_f32_e32 v201, v201
	v_rcp_f32_e32 v203, v203
	v_fmamk_f32 v204, v202, 0xc0b8aa3b, v222
	v_mul_f32_e32 v205, v200, v204
	v_fma_f32 v220, v201, v220, v205
	v_exp_f32_e32 v206, v220
	v_mul_f32_e32 v207, -2.0, v203
	v_add_f32_e32 v206, 1.0, v206
	v_rcp_f32_e32 v206, v206
	v_max_f32_e32 v221, v221, v215
	v_fma_mixlo_f16 v208, v206, v207, v203
	ds_write_b16 v225, v208 offset:640
	v_fma_f32 v215, v206, v207, v203
	v_mfma_f32_16x16x32_f16 v[232:235], v[80:83], v[128:131], v[120:123]
	v_mfma_f32_16x16x32_f16 v[164:167], v[72:75], v[136:139], v[164:167]
	ds_write_b128 v227, v[160:163] offset:0
	ds_read_b128 v[196:199], v226 offset:5440
	s_waitcnt lgkmcnt(2)
	s_barrier
	ds_read_b128 v[184:187], v210 offset:640
	ds_read_b128 v[188:191], v210 offset:704
	ds_read_b128 v[176:179], v212 offset:640
	ds_read_b128 v[180:183], v212 offset:704
	v_mfma_f32_16x16x32_f16 v[232:235], v[84:87], v[132:135], v[232:235]
	v_mfma_f32_16x16x32_f16 v[164:167], v[76:79], v[140:143], v[164:167]
	s_waitcnt lgkmcnt(3)
	v_mfma_f32_16x16x32_f16 v[168:171], v[16:19], v[184:187], v[196:199]
	v_mfma_f32_16x16x32_f16 v[172:175], v[24:27], v[184:187], v[196:199]
	s_waitcnt lgkmcnt(2)
	v_mfma_f32_16x16x32_f16 v[168:171], v[20:23], v[188:191], v[168:171]
	v_mfma_f32_16x16x32_f16 v[172:175], v[28:31], v[188:191], v[172:175]
	s_waitcnt lgkmcnt(1)
	v_mfma_f32_16x16x32_f16 v[168:171], v[32:35], v[176:179], v[168:171]
	v_mfma_f32_16x16x32_f16 v[172:175], v[40:43], v[176:179], v[172:175]
	s_waitcnt lgkmcnt(0)
	v_mfma_f32_16x16x32_f16 v[168:171], v[36:39], v[180:183], v[168:171]
	v_mfma_f32_16x16x32_f16 v[172:175], v[44:47], v[180:183], v[172:175]
	s_nop 7
	v_mov_b32_dpp v168, v172 quad_perm:[0,1,2,3] row_mask:0xf bank_mask:0xa
	v_mov_b32_dpp v169, v173 quad_perm:[0,1,2,3] row_mask:0xf bank_mask:0xa
	v_mov_b32_dpp v170, v174 quad_perm:[0,1,2,3] row_mask:0xf bank_mask:0xa
	v_exp_f32_e32 v200, v168
	v_mov_b32_dpp v171, v175 quad_perm:[0,1,2,3] row_mask:0xf bank_mask:0xa
	v_exp_f32_e32 v201, v169
	v_exp_f32_e32 v202, v170
	v_exp_f32_e32 v203, v171
	v_pk_add_f32 v[200:201], v[200:201], 1.0 op_sel_hi:[1,0]
	v_pk_add_f32 v[202:203], v[202:203], 1.0 op_sel_hi:[1,0]
	v_rcp_f32_e32 v202, v202
	v_rcp_f32_e32 v200, v200
	v_rcp_f32_e32 v201, v201
	v_rcp_f32_e32 v203, v203
	v_fmamk_f32 v204, v202, 0xc0b8aa3b, v222
	v_mul_f32_e32 v205, v200, v204
	v_fma_f32 v220, v201, v220, v205
	v_exp_f32_e32 v206, v220
	v_mul_f32_e32 v207, -2.0, v203
	v_add_f32_e32 v206, 1.0, v206
	v_rcp_f32_e32 v206, v206
	v_max_f32_e32 v221, v221, v215
	v_fma_mixlo_f16 v208, v206, v207, v203
	ds_write_b16 v225, v208 offset:0
	v_fma_f32 v215, v206, v207, v203
	v_mfma_f32_16x16x32_f16 v[236:239], v[96:99], v[128:131], v[124:127]
	v_mfma_f32_16x16x32_f16 v[232:235], v[88:91], v[136:139], v[232:235]
	global_load_dwordx4 v[128:131], v[228:229], off offset:0
	ds_write_b128 v227, v[164:167] offset:64
	ds_read_b128 v[192:195], v226 offset:6528
	s_waitcnt lgkmcnt(2)
	s_barrier
	ds_read_b128 v[184:187], v209 offset:0
	ds_read_b128 v[188:191], v209 offset:64
	ds_read_b128 v[176:179], v211 offset:0
	ds_read_b128 v[180:183], v211 offset:64
	v_mfma_f32_16x16x32_f16 v[236:239], v[100:103], v[132:135], v[236:239]
	v_mfma_f32_16x16x32_f16 v[232:235], v[92:95], v[140:143], v[232:235]
	global_load_dwordx4 v[132:135], v[228:229], off offset:64
	s_waitcnt lgkmcnt(3)
	v_mfma_f32_16x16x32_f16 v[168:171], v[16:19], v[184:187], v[192:195]
	v_mfma_f32_16x16x32_f16 v[172:175], v[24:27], v[184:187], v[192:195]
	s_waitcnt lgkmcnt(2)
	v_mfma_f32_16x16x32_f16 v[168:171], v[20:23], v[188:191], v[168:171]
	v_mfma_f32_16x16x32_f16 v[172:175], v[28:31], v[188:191], v[172:175]
	s_waitcnt lgkmcnt(1)
	v_mfma_f32_16x16x32_f16 v[168:171], v[32:35], v[176:179], v[168:171]
	v_mfma_f32_16x16x32_f16 v[172:175], v[40:43], v[176:179], v[172:175]
	s_waitcnt lgkmcnt(0)
	v_mfma_f32_16x16x32_f16 v[168:171], v[36:39], v[180:183], v[168:171]
	v_mfma_f32_16x16x32_f16 v[172:175], v[44:47], v[180:183], v[172:175]
	s_nop 7
	v_mov_b32_dpp v168, v172 quad_perm:[0,1,2,3] row_mask:0xf bank_mask:0xa
	v_mov_b32_dpp v169, v173 quad_perm:[0,1,2,3] row_mask:0xf bank_mask:0xa
	v_mov_b32_dpp v170, v174 quad_perm:[0,1,2,3] row_mask:0xf bank_mask:0xa
	v_exp_f32_e32 v200, v168
	v_mov_b32_dpp v171, v175 quad_perm:[0,1,2,3] row_mask:0xf bank_mask:0xa
	v_exp_f32_e32 v201, v169
	v_exp_f32_e32 v202, v170
	v_exp_f32_e32 v203, v171
	v_pk_add_f32 v[200:201], v[200:201], 1.0 op_sel_hi:[1,0]
	v_pk_add_f32 v[202:203], v[202:203], 1.0 op_sel_hi:[1,0]
	v_rcp_f32_e32 v202, v202
	v_rcp_f32_e32 v200, v200
	v_rcp_f32_e32 v201, v201
	v_rcp_f32_e32 v203, v203
	v_fmamk_f32 v204, v202, 0xc0b8aa3b, v222
	v_mul_f32_e32 v205, v200, v204
	v_fma_f32 v220, v201, v220, v205
	v_exp_f32_e32 v206, v220
	v_mul_f32_e32 v207, -2.0, v203
	v_add_f32_e32 v206, 1.0, v206
	v_rcp_f32_e32 v206, v206
	v_max_f32_e32 v221, v221, v215
	v_fma_mixlo_f16 v208, v206, v207, v203
	ds_write_b16 v225, v208 offset:640
	v_fma_f32 v215, v206, v207, v203
	s_waitcnt vmcnt(5)
	v_mfma_f32_16x16x32_f16 v[160:163], v[48:51], v[144:147], v[112:115]
	v_mfma_f32_16x16x32_f16 v[236:239], v[104:107], v[136:139], v[236:239]
	global_load_dwordx4 v[136:139], v[228:229], off offset:128
	ds_write_b128 v227, v[232:235] offset:128
	ds_read_b128 v[196:199], v226 offset:7616
	s_waitcnt lgkmcnt(2)
	s_barrier
	ds_read_b128 v[184:187], v210 offset:640
	ds_read_b128 v[188:191], v210 offset:704
	ds_read_b128 v[176:179], v212 offset:640
	ds_read_b128 v[180:183], v212 offset:704
	s_waitcnt vmcnt(5)
	v_mfma_f32_16x16x32_f16 v[160:163], v[52:55], v[148:151], v[160:163]
	v_mfma_f32_16x16x32_f16 v[236:239], v[108:111], v[140:143], v[236:239]
	global_load_dwordx4 v[140:143], v[228:229], off offset:192
	v_lshl_add_u64 v[228:229], v[228:229], 0, s[20:21]
	s_waitcnt lgkmcnt(3)
	v_mfma_f32_16x16x32_f16 v[168:171], v[16:19], v[184:187], v[196:199]
	v_mfma_f32_16x16x32_f16 v[172:175], v[24:27], v[184:187], v[196:199]
	s_waitcnt lgkmcnt(2)
	v_mfma_f32_16x16x32_f16 v[168:171], v[20:23], v[188:191], v[168:171]
	v_mfma_f32_16x16x32_f16 v[172:175], v[28:31], v[188:191], v[172:175]
	s_waitcnt lgkmcnt(1)
	v_mfma_f32_16x16x32_f16 v[168:171], v[32:35], v[176:179], v[168:171]
	v_mfma_f32_16x16x32_f16 v[172:175], v[40:43], v[176:179], v[172:175]
	s_waitcnt lgkmcnt(0)
	v_mfma_f32_16x16x32_f16 v[168:171], v[36:39], v[180:183], v[168:171]
	v_mfma_f32_16x16x32_f16 v[172:175], v[44:47], v[180:183], v[172:175]
	s_nop 7
	v_mov_b32_dpp v168, v172 quad_perm:[0,1,2,3] row_mask:0xf bank_mask:0xa
	v_mov_b32_dpp v169, v173 quad_perm:[0,1,2,3] row_mask:0xf bank_mask:0xa
	v_mov_b32_dpp v170, v174 quad_perm:[0,1,2,3] row_mask:0xf bank_mask:0xa
	v_exp_f32_e32 v200, v168
	v_mov_b32_dpp v171, v175 quad_perm:[0,1,2,3] row_mask:0xf bank_mask:0xa
	v_exp_f32_e32 v201, v169
	v_exp_f32_e32 v202, v170
	v_exp_f32_e32 v203, v171
	v_pk_add_f32 v[200:201], v[200:201], 1.0 op_sel_hi:[1,0]
	v_pk_add_f32 v[202:203], v[202:203], 1.0 op_sel_hi:[1,0]
	v_rcp_f32_e32 v202, v202
	v_rcp_f32_e32 v200, v200
	v_rcp_f32_e32 v201, v201
	v_rcp_f32_e32 v203, v203
	v_fmamk_f32 v204, v202, 0xc0b8aa3b, v222
	v_mul_f32_e32 v205, v200, v204
	v_fma_f32 v220, v201, v220, v205
	v_exp_f32_e32 v206, v220
	v_mul_f32_e32 v207, -2.0, v203
	v_add_f32_e32 v206, 1.0, v206
	v_rcp_f32_e32 v206, v206
	v_max_f32_e32 v221, v221, v215
	v_fma_mixlo_f16 v208, v206, v207, v203
	ds_write_b16 v225, v208 offset:0
	v_fma_f32 v215, v206, v207, v203
	v_mfma_f32_16x16x32_f16 v[164:167], v[64:67], v[144:147], v[116:119]
	s_waitcnt vmcnt(5)
	v_mfma_f32_16x16x32_f16 v[160:163], v[56:59], v[152:155], v[160:163]
	ds_write_b128 v227, v[236:239] offset:192
	ds_read_b128 v[192:195], v226 offset:0
	s_waitcnt lgkmcnt(2)
	s_barrier
	s_sub_u32 s4, s4, 1
	s_cmp_lg_u32 s4, 0
	s_cbranch_scc1 .Llstm3_loop
	v_max_f32_e32 v221, v221, v215
	global_store_dword v230, v221, s[12:13]
	s_endpgm

	.amdhsa_kernel _Z12lstm2_kernelPKDF16_PKDv8_DF16_Pf
		.amdhsa_group_segment_fixed_size 36224
		.amdhsa_private_segment_fixed_size 0
		.amdhsa_kernarg_size 24
		.amdhsa_user_sgpr_count 2
		.amdhsa_user_sgpr_dispatch_ptr 0
		.amdhsa_user_sgpr_queue_ptr 0
		.amdhsa_user_sgpr_kernarg_segment_ptr 1
		.amdhsa_user_sgpr_dispatch_id 0
		.amdhsa_user_sgpr_kernarg_preload_length 0
		.amdhsa_user_sgpr_kernarg_preload_offset 0
		.amdhsa_user_sgpr_private_segment_size 0
		.amdhsa_uses_dynamic_stack 0
		.amdhsa_enable_private_segment 0
		.amdhsa_system_sgpr_workgroup_id_x 1
		.amdhsa_system_sgpr_workgroup_id_y 0
		.amdhsa_system_sgpr_workgroup_id_z 0
		.amdhsa_system_sgpr_workgroup_info 0
		.amdhsa_system_vgpr_workitem_id 0
		.amdhsa_next_free_vgpr 252
		.amdhsa_next_free_sgpr 32
		.amdhsa_accum_offset 252
		.amdhsa_reserve_vcc 1
		.amdhsa_float_round_mode_32 0
		.amdhsa_float_round_mode_16_64 0
		.amdhsa_float_denorm_mode_32 3
		.amdhsa_float_denorm_mode_16_64 3
		.amdhsa_dx10_clamp 1
		.amdhsa_ieee_mode 1
		.amdhsa_fp16_overflow 0
		.amdhsa_tg_split 0
		.amdhsa_exception_fp_ieee_invalid_op 0
		.amdhsa_exception_fp_denorm_src 0
		.amdhsa_exception_fp_ieee_div_zero 0
		.amdhsa_exception_fp_ieee_overflow 0
		.amdhsa_exception_fp_ieee_underflow 0
		.amdhsa_exception_fp_ieee_inexact 0
		.amdhsa_exception_int_div_zero 0
	.end_amdhsa_kernel

amdhsa.kernels:
  - .agpr_count:     0
    .args:
      - .actual_access:  write_only
        .address_space:  global
        .offset:         0
        .size:           8
        .value_kind:     global_buffer
      - .actual_access:  read_only
        .address_space:  global
        .offset:         8
        .size:           8
        .value_kind:     global_buffer
      - .actual_access:  read_only
        .address_space:  global
        .offset:         16
        .size:           8
        .value_kind:     global_buffer
      - .actual_access:  read_only
        .address_space:  global
        .offset:         24
        .size:           8
        .value_kind:     global_buffer
      - .actual_access:  read_only
        .address_space:  global
        .offset:         32
        .size:           8
        .value_kind:     global_buffer
      - .actual_access:  read_only
        .address_space:  global
        .offset:         40
        .size:           8
        .value_kind:     global_buffer
      - .actual_access:  read_only
        .address_space:  global
        .offset:         48
        .size:           8
        .value_kind:     global_buffer
      - .actual_access:  read_only
        .address_space:  global
        .offset:         56
        .size:           8
        .value_kind:     global_buffer
      - .actual_access:  read_only
        .address_space:  global
        .offset:         64
        .size:           8
        .value_kind:     global_buffer
      - .actual_access:  read_only
        .address_space:  global
        .offset:         72
        .size:           8
        .value_kind:     global_buffer
    .group_segment_fixed_size: 0
    .kernarg_segment_align: 8
    .kernarg_segment_size: 80
    .language:       OpenCL C
    .language_version:
      - 2
      - 0
    .max_flat_workgroup_size: 64
    .name:           _Z11prep_kernelPDv8_DF16_PKfS2_S2_S2_S2_S2_S2_S2_S2_
    .private_segment_fixed_size: 0
    .sgpr_count:     20
    .sgpr_spill_count: 0
    .symbol:         _Z11prep_kernelPDv8_DF16_PKfS2_S2_S2_S2_S2_S2_S2_S2_.kd
    .uniform_work_group_size: 1
    .uses_dynamic_stack: false
    .vgpr_count:     18
    .vgpr_spill_count: 0
    .wavefront_size: 64
  - .agpr_count:     0
    .args:
      - .actual_access:  read_only
        .address_space:  global
        .offset:         0
        .size:           8
        .value_kind:     global_buffer
      - .actual_access:  read_only
        .address_space:  global
        .offset:         8
        .size:           8
        .value_kind:     global_buffer
      - .actual_access:  write_only
        .address_space:  global
        .offset:         16
        .size:           8
        .value_kind:     global_buffer
    .group_segment_fixed_size: 0
    .kernarg_segment_align: 8
    .kernarg_segment_size: 24
    .language:       OpenCL C
    .language_version:
      - 2
      - 0
    .max_flat_workgroup_size: 256
    .name:           _Z11init_kernelPKfS0_PDF16_
    .private_segment_fixed_size: 0
    .sgpr_count:     16
    .sgpr_spill_count: 0
    .symbol:         _Z11init_kernelPKfS0_PDF16_.kd
    .uniform_work_group_size: 1
    .uses_dynamic_stack: false
    .vgpr_count:     118
    .vgpr_spill_count: 0
    .wavefront_size: 64
  - .agpr_count:     0
    .args:
      - .actual_access:  read_only
        .address_space:  global
        .offset:         0
        .size:           8
        .value_kind:     global_buffer
      - .actual_access:  write_only
        .address_space:  global
        .offset:         8
        .size:           8
        .value_kind:     global_buffer
      - .actual_access:  read_only
        .address_space:  global
        .offset:         16
        .size:           8
        .value_kind:     global_buffer
      - .actual_access:  read_only
        .address_space:  global
        .offset:         24
        .size:           8
        .value_kind:     global_buffer
      - .actual_access:  read_only
        .address_space:  global
        .offset:         32
        .size:           8
        .value_kind:     global_buffer
      - .actual_access:  read_only
        .address_space:  global
        .offset:         40
        .size:           8
        .value_kind:     global_buffer
      - .actual_access:  read_only
        .address_space:  global
        .offset:         48
        .size:           8
        .value_kind:     global_buffer
      - .offset:         56
        .size:           4
        .value_kind:     by_value
      - .offset:         64
        .size:           4
        .value_kind:     hidden_block_count_x
      - .offset:         68
        .size:           4
        .value_kind:     hidden_block_count_y
      - .offset:         72
        .size:           4
        .value_kind:     hidden_block_count_z
      - .offset:         76
        .size:           2
        .value_kind:     hidden_group_size_x
      - .offset:         78
        .size:           2
        .value_kind:     hidden_group_size_y
      - .offset:         80
        .size:           2
        .value_kind:     hidden_group_size_z
      - .offset:         82
        .size:           2
        .value_kind:     hidden_remainder_x
      - .offset:         84
        .size:           2
        .value_kind:     hidden_remainder_y
      - .offset:         86
        .size:           2
        .value_kind:     hidden_remainder_z
      - .offset:         104
        .size:           8
        .value_kind:     hidden_global_offset_x
      - .offset:         112
        .size:           8
        .value_kind:     hidden_global_offset_y
      - .offset:         120
        .size:           8
        .value_kind:     hidden_global_offset_z
      - .offset:         128
        .size:           2
        .value_kind:     hidden_grid_dims
      - .offset:         184
        .size:           4
        .value_kind:     hidden_dynamic_lds_size
    .group_segment_fixed_size: 0
    .kernarg_segment_align: 8
    .kernarg_segment_size: 320
    .language:       OpenCL C
    .language_version:
      - 2
      - 0
    .max_flat_workgroup_size: 512
    .name:           _Z12xproj_kernelPKDF16_PDF16_PKDv8_DF16_PKfS6_S6_S6_i
    .private_segment_fixed_size: 0
    .sgpr_count:     30
    .sgpr_spill_count: 0
    .symbol:         _Z12xproj_kernelPKDF16_PDF16_PKDv8_DF16_PKfS6_S6_S6_i.kd
    .uniform_work_group_size: 1
    .uses_dynamic_stack: false
    .vgpr_count:     16
    .vgpr_spill_count: 0
    .wavefront_size: 64
  - .agpr_count:     0
    .args:
      - .actual_access:  read_only
        .address_space:  global
        .offset:         0
        .size:           8
        .value_kind:     global_buffer
      - .actual_access:  read_only
        .address_space:  global
        .offset:         8
        .size:           8
        .value_kind:     global_buffer
      - .actual_access:  write_only
        .address_space:  global
        .offset:         16
        .size:           8
        .value_kind:     global_buffer
    .group_segment_fixed_size: 5120
    .kernarg_segment_align: 8
    .kernarg_segment_size: 24
    .language:       OpenCL C
    .language_version:
      - 2
      - 0
    .max_flat_workgroup_size: 1024
    .name:           _Z11lstm_kernelPKDF16_PKDv8_DF16_Pf
    .private_segment_fixed_size: 0
    .sgpr_count:     18
    .sgpr_spill_count: 0
    .symbol:         _Z11lstm_kernelPKDF16_PKDv8_DF16_Pf.kd
    .uniform_work_group_size: 1
    .uses_dynamic_stack: false
    .vgpr_count:     52
    .vgpr_spill_count: 0
    .wavefront_size: 64
  - .agpr_count:     0
    .args:
      - .actual_access:  read_only
        .address_space:  global
        .offset:         0
        .size:           8
        .value_kind:     global_buffer
      - .actual_access:  read_only
        .address_space:  global
        .offset:         8
        .size:           8
        .value_kind:     global_buffer
      - .actual_access:  write_only
        .address_space:  global
        .offset:         16
        .size:           8
        .value_kind:     global_buffer
    .group_segment_fixed_size: 36224
    .kernarg_segment_align: 8
    .kernarg_segment_size: 24
    .language:       OpenCL C
    .language_version:
      - 2
      - 0
    .max_flat_workgroup_size: 256
    .name:           _Z12lstm2_kernelPKDF16_PKDv8_DF16_Pf
    .private_segment_fixed_size: 0
    .sgpr_count:     38
    .sgpr_spill_count: 0
    .symbol:         _Z12lstm2_kernelPKDF16_PKDv8_DF16_Pf.kd
    .uniform_work_group_size: 1
    .uses_dynamic_stack: false
    .vgpr_count:     252
    .vgpr_spill_count: 0
    .wavefront_size: 64
  - .agpr_count:     0
    .args:
      - .address_space:  global
        .offset:         0
        .size:           8
        .value_kind:     global_buffer
      - .actual_access:  write_only
        .address_space:  global
        .offset:         8
        .size:           8
        .value_kind:     global_buffer
      - .address_space:  global
        .offset:         16
        .size:           8
        .value_kind:     global_buffer
      - .address_space:  global
        .offset:         24
        .size:           8
        .value_kind:     global_buffer
      - .actual_access:  read_only
        .address_space:  global
        .offset:         32
        .size:           8
        .value_kind:     global_buffer
      - .actual_access:  read_only
        .address_space:  global
        .offset:         40
        .size:           8
        .value_kind:     global_buffer
      - .actual_access:  read_only
        .address_space:  global
        .offset:         48
        .size:           8
        .value_kind:     global_buffer
      - .offset:         56
        .size:           4
        .value_kind:     by_value
      - .offset:         60
        .size:           4
        .value_kind:     by_value
      - .offset:         64
        .size:           4
        .value_kind:     hidden_block_count_x
      - .offset:         68
        .size:           4
        .value_kind:     hidden_block_count_y
      - .offset:         72
        .size:           4
        .value_kind:     hidden_block_count_z
      - .offset:         76
        .size:           2
        .value_kind:     hidden_group_size_x
      - .offset:         78
        .size:           2
        .value_kind:     hidden_group_size_y
      - .offset:         80
        .size:           2
        .value_kind:     hidden_group_size_z
      - .offset:         82
        .size:           2
        .value_kind:     hidden_remainder_x
      - .offset:         84
        .size:           2
        .value_kind:     hidden_remainder_y
      - .offset:         86
        .size:           2
        .value_kind:     hidden_remainder_z
      - .offset:         104
        .size:           8
        .value_kind:     hidden_global_offset_x
      - .offset:         112
        .size:           8
        .value_kind:     hidden_global_offset_y
      - .offset:         120
        .size:           8
        .value_kind:     hidden_global_offset_z
      - .offset:         128
        .size:           2
        .value_kind:     hidden_grid_dims
      - .offset:         184
        .size:           4
        .value_kind:     hidden_dynamic_lds_size
    .group_segment_fixed_size: 0
    .kernarg_segment_align: 8
    .kernarg_segment_size: 320
    .language:       OpenCL C
    .language_version:
      - 2
      - 0
    .max_flat_workgroup_size: 512
    .name:           _Z10mp2_kernelILb0ELi0EEvPKDF16_PDF16_PKiPKfPKDv8_DF16_S6_S6_ii
    .private_segment_fixed_size: 0
    .sgpr_count:     54
    .sgpr_spill_count: 0
    .symbol:         _Z10mp2_kernelILb0ELi0EEvPKDF16_PDF16_PKiPKfPKDv8_DF16_S6_S6_ii.kd
    .uniform_work_group_size: 1
    .uses_dynamic_stack: false
    .vgpr_count:     244
    .vgpr_spill_count: 0
    .wavefront_size: 64
  - .agpr_count:     0
    .args:
      - .actual_access:  read_only
        .address_space:  global
        .offset:         0
        .size:           8
        .value_kind:     global_buffer
      - .actual_access:  write_only
        .address_space:  global
        .offset:         8
        .size:           8
        .value_kind:     global_buffer
      - .address_space:  global
        .offset:         16
        .size:           8
        .value_kind:     global_buffer
      - .address_space:  global
        .offset:         24
        .size:           8
        .value_kind:     global_buffer
      - .actual_access:  read_only
        .address_space:  global
        .offset:         32
        .size:           8
        .value_kind:     global_buffer
      - .actual_access:  read_only
        .address_space:  global
        .offset:         40
        .size:           8
        .value_kind:     global_buffer
      - .actual_access:  read_only
        .address_space:  global
        .offset:         48
        .size:           8
        .value_kind:     global_buffer
      - .offset:         56
        .size:           4
        .value_kind:     by_value
      - .offset:         60
        .size:           4
        .value_kind:     by_value
      - .offset:         64
        .size:           4
        .value_kind:     hidden_block_count_x
      - .offset:         68
        .size:           4
        .value_kind:     hidden_block_count_y
      - .offset:         72
        .size:           4
        .value_kind:     hidden_block_count_z
      - .offset:         76
        .size:           2
        .value_kind:     hidden_group_size_x
      - .offset:         78
        .size:           2
        .value_kind:     hidden_group_size_y
      - .offset:         80
        .size:           2
        .value_kind:     hidden_group_size_z
      - .offset:         82
        .size:           2
        .value_kind:     hidden_remainder_x
      - .offset:         84
        .size:           2
        .value_kind:     hidden_remainder_y
      - .offset:         86
        .size:           2
        .value_kind:     hidden_remainder_z
      - .offset:         104
        .size:           8
        .value_kind:     hidden_global_offset_x
      - .offset:         112
        .size:           8
        .value_kind:     hidden_global_offset_y
      - .offset:         120
        .size:           8
        .value_kind:     hidden_global_offset_z
      - .offset:         128
        .size:           2
        .value_kind:     hidden_grid_dims
      - .offset:         184
        .size:           4
        .value_kind:     hidden_dynamic_lds_size
    .group_segment_fixed_size: 0
    .kernarg_segment_align: 8
    .kernarg_segment_size: 320
    .language:       OpenCL C
    .language_version:
      - 2
      - 0
    .max_flat_workgroup_size: 512
    .name:           _Z10mp2_kernelILb0ELi1EEvPKDF16_PDF16_PKiPKfPKDv8_DF16_S6_S6_ii
    .private_segment_fixed_size: 0
    .sgpr_count:     32
    .sgpr_spill_count: 0
    .symbol:         _Z10mp2_kernelILb0ELi1EEvPKDF16_PDF16_PKiPKfPKDv8_DF16_S6_S6_ii.kd
    .uniform_work_group_size: 1
    .uses_dynamic_stack: false
    .vgpr_count:     234
    .vgpr_spill_count: 0
    .wavefront_size: 64
  - .agpr_count:     0
    .args:
      - .address_space:  global
        .offset:         0
        .size:           8
        .value_kind:     global_buffer
      - .actual_access:  write_only
        .address_space:  global
        .offset:         8
        .size:           8
        .value_kind:     global_buffer
      - .actual_access:  read_only
        .address_space:  global
        .offset:         16
        .size:           8
        .value_kind:     global_buffer
      - .actual_access:  read_only
        .address_space:  global
        .offset:         24
        .size:           8
        .value_kind:     global_buffer
      - .actual_access:  read_only
        .address_space:  global
        .offset:         32
        .size:           8
        .value_kind:     global_buffer
      - .actual_access:  read_only
        .address_space:  global
        .offset:         40
        .size:           8
        .value_kind:     global_buffer
      - .actual_access:  read_only
        .address_space:  global
        .offset:         48
        .size:           8
        .value_kind:     global_buffer
      - .offset:         56
        .size:           4
        .value_kind:     by_value
      - .offset:         60
        .size:           4
        .value_kind:     by_value
      - .offset:         64
        .size:           4
        .value_kind:     hidden_block_count_x
      - .offset:         68
        .size:           4
        .value_kind:     hidden_block_count_y
      - .offset:         72
        .size:           4
        .value_kind:     hidden_block_count_z
      - .offset:         76
        .size:           2
        .value_kind:     hidden_group_size_x
      - .offset:         78
        .size:           2
        .value_kind:     hidden_group_size_y
      - .offset:         80
        .size:           2
        .value_kind:     hidden_group_size_z
      - .offset:         82
        .size:           2
        .value_kind:     hidden_remainder_x
      - .offset:         84
        .size:           2
        .value_kind:     hidden_remainder_y
      - .offset:         86
        .size:           2
        .value_kind:     hidden_remainder_z
      - .offset:         104
        .size:           8
        .value_kind:     hidden_global_offset_x
      - .offset:         112
        .size:           8
        .value_kind:     hidden_global_offset_y
      - .offset:         120
        .size:           8
        .value_kind:     hidden_global_offset_z
      - .offset:         128
        .size:           2
        .value_kind:     hidden_grid_dims
      - .offset:         184
        .size:           4
        .value_kind:     hidden_dynamic_lds_size
    .group_segment_fixed_size: 0
    .kernarg_segment_align: 8
    .kernarg_segment_size: 320
    .language:       OpenCL C
    .language_version:
      - 2
      - 0
    .max_flat_workgroup_size: 512
    .name:           _Z9mp_kernelILi1EEvPKDF16_PDF16_PKiPKfPKDv8_DF16_S6_S6_ii
    .private_segment_fixed_size: 0
    .sgpr_count:     46
    .sgpr_spill_count: 0
    .symbol:         _Z9mp_kernelILi1EEvPKDF16_PDF16_PKiPKfPKDv8_DF16_S6_S6_ii.kd
    .uniform_work_group_size: 1
    .uses_dynamic_stack: false
    .vgpr_count:     70
    .vgpr_spill_count: 0
    .wavefront_size: 64
  - .agpr_count:     0
    .args:
      - .address_space:  global
        .offset:         0
        .size:           8
        .value_kind:     global_buffer
      - .actual_access:  write_only
        .address_space:  global
        .offset:         8
        .size:           8
        .value_kind:     global_buffer
      - .address_space:  global
        .offset:         16
        .size:           8
        .value_kind:     global_buffer
      - .address_space:  global
        .offset:         24
        .size:           8
        .value_kind:     global_buffer
      - .actual_access:  read_only
        .address_space:  global
        .offset:         32
        .size:           8
        .value_kind:     global_buffer
      - .actual_access:  read_only
        .address_space:  global
        .offset:         40
        .size:           8
        .value_kind:     global_buffer
      - .actual_access:  read_only
        .address_space:  global
        .offset:         48
        .size:           8
        .value_kind:     global_buffer
      - .offset:         56
        .size:           4
        .value_kind:     by_value
      - .offset:         60
        .size:           4
        .value_kind:     by_value
      - .offset:         64
        .size:           4
        .value_kind:     hidden_block_count_x
      - .offset:         68
        .size:           4
        .value_kind:     hidden_block_count_y
      - .offset:         72
        .size:           4
        .value_kind:     hidden_block_count_z
      - .offset:         76
        .size:           2
        .value_kind:     hidden_group_size_x
      - .offset:         78
        .size:           2
        .value_kind:     hidden_group_size_y
      - .offset:         80
        .size:           2
        .value_kind:     hidden_group_size_z
      - .offset:         82
        .size:           2
        .value_kind:     hidden_remainder_x
      - .offset:         84
        .size:           2
        .value_kind:     hidden_remainder_y
      - .offset:         86
        .size:           2
        .value_kind:     hidden_remainder_z
      - .offset:         104
        .size:           8
        .value_kind:     hidden_global_offset_x
      - .offset:         112
        .size:           8
        .value_kind:     hidden_global_offset_y
      - .offset:         120
        .size:           8
        .value_kind:     hidden_global_offset_z
      - .offset:         128
        .size:           2
        .value_kind:     hidden_grid_dims
      - .offset:         184
        .size:           4
        .value_kind:     hidden_dynamic_lds_size
    .group_segment_fixed_size: 0
    .kernarg_segment_align: 8
    .kernarg_segment_size: 320
    .language:       OpenCL C
    .language_version:
      - 2
      - 0
    .max_flat_workgroup_size: 512
    .name:           _Z10mp2_kernelILb0ELi2EEvPKDF16_PDF16_PKiPKfPKDv8_DF16_S6_S6_ii
    .private_segment_fixed_size: 0
    .sgpr_count:     34
    .sgpr_spill_count: 0
    .symbol:         _Z10mp2_kernelILb0ELi2EEvPKDF16_PDF16_PKiPKfPKDv8_DF16_S6_S6_ii.kd
    .uniform_work_group_size: 1
    .uses_dynamic_stack: false
    .vgpr_count:     99
    .vgpr_spill_count: 0
    .wavefront_size: 64
